# P10: cooperative L2 prefetch - each wave's one throw-away load in the epilogue touches a distinct 8 KB slice of the next unit's shared A tile / B slab
# speedup vs baseline: 1.0547x; 1.0139x over previous
.LBB0_1441:
	s_and_b64 vcc, exec, s[0:1]
	s_cmp_eq_u32 s98, 0
	s_cbranch_scc1 .Lgk_first_p10
	v_mov_b32_e32 v175, v169
	v_mov_b32_e32 v173, v169
	s_mov_b32 s23, 0
	s_mov_b64 s[34:35], 0x100
	s_mov_b64 s[36:37], s[16:17]
	ds_read_b128 v[26:29], v191
	ds_read_b128 v[30:33], v191 offset:1024
	ds_read_b128 v[18:21], v191 offset:2048
	ds_read_b128 v[22:25], v191 offset:3072
	ds_read_b128 v[10:13], v192
	ds_read_b128 v[14:17], v192 offset:1024
	ds_read_b128 v[2:5], v192 offset:2048
	ds_read_b128 v[6:9], v192 offset:3072
	s_cmp_eq_u32 s54, s23
	s_cselect_b64 vcc, -1, 0
	s_add_i32 s23, s23, 2
	s_and_b64 s[38:39], vcc, exec
	s_cselect_b32 s38, 0, s34
	s_cselect_b32 s25, 0, s35
	s_add_u32 s38, s12, s38
	s_addc_u32 s39, s13, s25
	s_add_u32 s25, s30, s34
	s_addc_u32 s67, s31, s35
	s_and_b64 s[40:41], vcc, exec
	v_cndmask_b32_e32 v168, v197, v198, vcc
	v_cndmask_b32_e32 v202, v172, v200, vcc
	v_cndmask_b32_e32 v184, v170, v199, vcc
	s_cselect_b32 s41, s27, s67
	s_cselect_b32 s40, s26, s25
	s_mov_b32 m0, s55
	v_lshl_add_u64 v[186:187], s[36:37], 0, v[172:173]
	ds_read_b128 v[176:179], v193
	ds_read_b128 v[180:183], v193 offset:1024
	ds_read_b128 v[208:211], v193 offset:2048
	ds_read_b128 v[212:215], v193 offset:3072
	ds_read_b128 v[216:219], v193 offset:4096
	ds_read_b128 v[220:223], v193 offset:5120
	ds_read_b128 v[224:227], v193 offset:6144
	ds_read_b128 v[228:231], v193 offset:7168
	global_load_lds_dwordx4 v[186:187], off
	v_lshl_add_u64 v[186:187], s[36:37], 0, v[174:175]
	s_mov_b32 m0, s56
	s_nop 0
	global_load_lds_dwordx4 v[186:187], off
	s_waitcnt vmcnt(17)
	s_waitcnt lgkmcnt(0)
	s_barrier
	s_setprio 1
	s_waitcnt lgkmcnt(0)
	v_mfma_scale_f32_16x16x128_f8f6f4 v[158:161], v[26:33], v[176:183], 0, v188, v189 op_sel_hi:[0,0,0]
	v_mfma_scale_f32_16x16x128_f8f6f4 v[154:157], v[18:25], v[176:183], 0, v188, v189 op_sel_hi:[0,0,0]
	v_mfma_scale_f32_16x16x128_f8f6f4 v[142:145], v[26:33], v[208:215], 0, v188, v189 op_sel_hi:[0,0,0]
	v_mfma_scale_f32_16x16x128_f8f6f4 v[138:141], v[18:25], v[208:215], 0, v188, v189 op_sel_hi:[0,0,0]
	v_mfma_scale_f32_16x16x128_f8f6f4 v[126:129], v[26:33], v[216:223], 0, v188, v189 op_sel_hi:[0,0,0]
	v_mfma_scale_f32_16x16x128_f8f6f4 v[122:125], v[18:25], v[216:223], 0, v188, v189 op_sel_hi:[0,0,0]
	v_mfma_scale_f32_16x16x128_f8f6f4 v[110:113], v[26:33], v[224:231], 0, v188, v189 op_sel_hi:[0,0,0]
	v_mfma_scale_f32_16x16x128_f8f6f4 v[106:109], v[18:25], v[224:231], 0, v188, v189 op_sel_hi:[0,0,0]
	s_setprio 0
	s_setprio 1
	v_mfma_scale_f32_16x16x128_f8f6f4 v[150:153], v[10:17], v[176:183], 0, v188, v189 op_sel_hi:[0,0,0]
	v_mfma_scale_f32_16x16x128_f8f6f4 v[146:149], v[2:9], v[176:183], 0, v188, v189 op_sel_hi:[0,0,0]
	v_mfma_scale_f32_16x16x128_f8f6f4 v[134:137], v[10:17], v[208:215], 0, v188, v189 op_sel_hi:[0,0,0]
	v_mfma_scale_f32_16x16x128_f8f6f4 v[130:133], v[2:9], v[208:215], 0, v188, v189 op_sel_hi:[0,0,0]
	v_mfma_scale_f32_16x16x128_f8f6f4 v[118:121], v[10:17], v[216:223], 0, v188, v189 op_sel_hi:[0,0,0]
	v_mfma_scale_f32_16x16x128_f8f6f4 v[114:117], v[2:9], v[216:223], 0, v188, v189 op_sel_hi:[0,0,0]
	v_mfma_scale_f32_16x16x128_f8f6f4 v[102:105], v[10:17], v[224:231], 0, v188, v189 op_sel_hi:[0,0,0]
	v_mfma_scale_f32_16x16x128_f8f6f4 v[98:101], v[2:9], v[224:231], 0, v188, v189 op_sel_hi:[0,0,0]
	s_setprio 0
	s_barrier
	s_mov_b32 m0, s57
	v_lshl_add_u64 v[176:177], s[40:41], 0, v[166:167]
	v_lshl_add_u64 v[178:179], s[40:41], 0, v[164:165]
	s_add_u32 s40, s40, s10
	ds_read_b128 v[208:211], v193 offset:16384
	ds_read_b128 v[212:215], v193 offset:17408
	ds_read_b128 v[216:219], v193 offset:18432
	ds_read_b128 v[220:223], v193 offset:19456
	ds_read_b128 v[224:227], v193 offset:20480
	ds_read_b128 v[228:231], v193 offset:21504
	ds_read_b128 v[232:235], v193 offset:22528
	ds_read_b128 v[236:239], v193 offset:23552
	global_load_lds_dwordx4 v[176:177], off
	s_mov_b32 m0, s58
	s_addc_u32 s41, s41, s11
	global_load_lds_dwordx4 v[178:179], off
	v_lshl_add_u64 v[180:181], s[40:41], 0, v[166:167]
	s_mov_b32 m0, s59
	v_lshl_add_u64 v[182:183], s[40:41], 0, v[164:165]
	global_load_lds_dwordx4 v[180:181], off
	s_mov_b32 m0, s60
	v_mov_b32_e32 v185, v169
	global_load_lds_dwordx4 v[182:183], off
	s_mov_b32 m0, s29
	v_lshl_add_u64 v[186:187], s[38:39], 0, v[168:169]
	global_load_lds_dwordx4 v168, s[38:39]
	s_mov_b32 m0, s46
	s_nop 0
	global_load_lds_dwordx4 v184, s[38:39]
	s_waitcnt vmcnt(17)
	s_waitcnt lgkmcnt(0)
	v_lshl_add_u64 v[184:185], s[38:39], 0, v[184:185]
	s_barrier
	s_setprio 1
	s_waitcnt lgkmcnt(0)
	v_mfma_scale_f32_16x16x128_f8f6f4 v[94:97], v[26:33], v[208:215], 0, v188, v189 op_sel_hi:[0,0,0]
	v_mfma_scale_f32_16x16x128_f8f6f4 v[90:93], v[18:25], v[208:215], 0, v188, v189 op_sel_hi:[0,0,0]
	v_mfma_scale_f32_16x16x128_f8f6f4 v[78:81], v[26:33], v[216:223], 0, v188, v189 op_sel_hi:[0,0,0]
	v_mfma_scale_f32_16x16x128_f8f6f4 v[74:77], v[18:25], v[216:223], 0, v188, v189 op_sel_hi:[0,0,0]
	v_mfma_scale_f32_16x16x128_f8f6f4 v[62:65], v[26:33], v[224:231], 0, v188, v189 op_sel_hi:[0,0,0]
	v_mfma_scale_f32_16x16x128_f8f6f4 v[58:61], v[18:25], v[224:231], 0, v188, v189 op_sel_hi:[0,0,0]
	v_mfma_scale_f32_16x16x128_f8f6f4 v[46:49], v[26:33], v[232:239], 0, v188, v189 op_sel_hi:[0,0,0]
	v_mfma_scale_f32_16x16x128_f8f6f4 v[42:45], v[18:25], v[232:239], 0, v188, v189 op_sel_hi:[0,0,0]
	s_setprio 0
	s_setprio 1
	v_mfma_scale_f32_16x16x128_f8f6f4 v[86:89], v[10:17], v[208:215], 0, v188, v189 op_sel_hi:[0,0,0]
	v_mfma_scale_f32_16x16x128_f8f6f4 v[82:85], v[2:9], v[208:215], 0, v188, v189 op_sel_hi:[0,0,0]
	v_mfma_scale_f32_16x16x128_f8f6f4 v[70:73], v[10:17], v[216:223], 0, v188, v189 op_sel_hi:[0,0,0]
	v_mfma_scale_f32_16x16x128_f8f6f4 v[66:69], v[2:9], v[216:223], 0, v188, v189 op_sel_hi:[0,0,0]
	v_mfma_scale_f32_16x16x128_f8f6f4 v[54:57], v[10:17], v[224:231], 0, v188, v189 op_sel_hi:[0,0,0]
	v_mfma_scale_f32_16x16x128_f8f6f4 v[50:53], v[2:9], v[224:231], 0, v188, v189 op_sel_hi:[0,0,0]
	v_mfma_scale_f32_16x16x128_f8f6f4 v[38:41], v[10:17], v[232:239], 0, v188, v189 op_sel_hi:[0,0,0]
	v_mfma_scale_f32_16x16x128_f8f6f4 v[34:37], v[2:9], v[232:239], 0, v188, v189 op_sel_hi:[0,0,0]
	s_setprio 0
	s_barrier
	ds_read_b128 v[26:29], v194
	ds_read_b128 v[30:33], v194 offset:1024
	ds_read_b128 v[18:21], v194 offset:2048
	ds_read_b128 v[22:25], v194 offset:3072
	ds_read_b128 v[10:13], v195
	ds_read_b128 v[14:17], v195 offset:1024
	ds_read_b128 v[2:5], v195 offset:2048
	ds_read_b128 v[6:9], v195 offset:3072
	s_mov_b32 m0, s47
	ds_read_b128 v[208:211], v193 offset:32768
	ds_read_b128 v[212:215], v193 offset:33792
	ds_read_b128 v[216:219], v193 offset:34816
	ds_read_b128 v[220:223], v193 offset:35840
	ds_read_b128 v[224:227], v193 offset:36864
	ds_read_b128 v[228:231], v193 offset:37888
	ds_read_b128 v[232:235], v193 offset:38912
	ds_read_b128 v[236:239], v193 offset:39936
	v_cndmask_b32_e32 v168, v174, v201, vcc
	global_load_lds_dwordx4 v202, s[38:39]
	s_mov_b32 m0, s48
	s_nop 0
	global_load_lds_dwordx4 v168, s[38:39]
	s_waitcnt vmcnt(8)
	s_waitcnt lgkmcnt(0)
	s_barrier
	s_setprio 1
	s_waitcnt lgkmcnt(0)
	v_mfma_scale_f32_16x16x128_f8f6f4 v[158:161], v[26:33], v[208:215], v[158:161], v188, v189 op_sel_hi:[0,0,0]
	v_mfma_scale_f32_16x16x128_f8f6f4 v[154:157], v[18:25], v[208:215], v[154:157], v188, v189 op_sel_hi:[0,0,0]
	v_mfma_scale_f32_16x16x128_f8f6f4 v[142:145], v[26:33], v[216:223], v[142:145], v188, v189 op_sel_hi:[0,0,0]
	v_mfma_scale_f32_16x16x128_f8f6f4 v[138:141], v[18:25], v[216:223], v[138:141], v188, v189 op_sel_hi:[0,0,0]
	v_mfma_scale_f32_16x16x128_f8f6f4 v[126:129], v[26:33], v[224:231], v[126:129], v188, v189 op_sel_hi:[0,0,0]
	v_mfma_scale_f32_16x16x128_f8f6f4 v[122:125], v[18:25], v[224:231], v[122:125], v188, v189 op_sel_hi:[0,0,0]
	v_mfma_scale_f32_16x16x128_f8f6f4 v[110:113], v[26:33], v[232:239], v[110:113], v188, v189 op_sel_hi:[0,0,0]
	v_mfma_scale_f32_16x16x128_f8f6f4 v[106:109], v[18:25], v[232:239], v[106:109], v188, v189 op_sel_hi:[0,0,0]
	s_setprio 0
	s_setprio 1
	v_mfma_scale_f32_16x16x128_f8f6f4 v[150:153], v[10:17], v[208:215], v[150:153], v188, v189 op_sel_hi:[0,0,0]
	v_mfma_scale_f32_16x16x128_f8f6f4 v[146:149], v[2:9], v[208:215], v[146:149], v188, v189 op_sel_hi:[0,0,0]
	v_mfma_scale_f32_16x16x128_f8f6f4 v[134:137], v[10:17], v[216:223], v[134:137], v188, v189 op_sel_hi:[0,0,0]
	v_mfma_scale_f32_16x16x128_f8f6f4 v[130:133], v[2:9], v[216:223], v[130:133], v188, v189 op_sel_hi:[0,0,0]
	v_mfma_scale_f32_16x16x128_f8f6f4 v[118:121], v[10:17], v[224:231], v[118:121], v188, v189 op_sel_hi:[0,0,0]
	v_mfma_scale_f32_16x16x128_f8f6f4 v[114:117], v[2:9], v[224:231], v[114:117], v188, v189 op_sel_hi:[0,0,0]
	v_mfma_scale_f32_16x16x128_f8f6f4 v[102:105], v[10:17], v[232:239], v[102:105], v188, v189 op_sel_hi:[0,0,0]
	v_mfma_scale_f32_16x16x128_f8f6f4 v[98:101], v[2:9], v[232:239], v[98:101], v188, v189 op_sel_hi:[0,0,0]
	s_setprio 0
	s_barrier
	s_mov_b32 m0, s61
	v_lshl_add_u64 v[176:177], v[176:177], 0, s[18:19]
	ds_read_b128 v[208:211], v193 offset:49152
	ds_read_b128 v[212:215], v193 offset:50176
	ds_read_b128 v[216:219], v193 offset:51200
	ds_read_b128 v[220:223], v193 offset:52224
	ds_read_b128 v[224:227], v193 offset:53248
	ds_read_b128 v[228:231], v193 offset:54272
	ds_read_b128 v[232:235], v193 offset:55296
	ds_read_b128 v[236:239], v193 offset:56320
	global_load_lds_dwordx4 v[176:177], off
	v_lshl_add_u64 v[176:177], v[178:179], 0, s[18:19]
	s_mov_b32 m0, s62
	s_nop 0
	global_load_lds_dwordx4 v[176:177], off
	v_lshl_add_u64 v[176:177], v[180:181], 0, s[18:19]
	s_mov_b32 m0, s63
	s_nop 0
	global_load_lds_dwordx4 v[176:177], off
	v_lshl_add_u64 v[176:177], v[182:183], 0, s[18:19]
	s_add_i32 m0, s63, 0x2000
	s_nop 0
	global_load_lds_dwordx4 v[176:177], off
	v_lshl_add_u64 v[176:177], v[186:187], 0, s[18:19]
	s_mov_b32 m0, s50
	s_nop 0
	global_load_lds_dwordx4 v[176:177], off
	v_lshl_add_u64 v[176:177], v[184:185], 0, s[18:19]
	s_mov_b32 m0, s51
	s_nop 0
	global_load_lds_dwordx4 v[176:177], off
	s_waitcnt vmcnt(8)
	s_waitcnt lgkmcnt(0)
	s_barrier
	s_setprio 1
	s_waitcnt lgkmcnt(0)
	v_mfma_scale_f32_16x16x128_f8f6f4 v[94:97], v[26:33], v[208:215], v[94:97], v188, v189 op_sel_hi:[0,0,0]
	v_mfma_scale_f32_16x16x128_f8f6f4 v[90:93], v[18:25], v[208:215], v[90:93], v188, v189 op_sel_hi:[0,0,0]
	v_mfma_scale_f32_16x16x128_f8f6f4 v[78:81], v[26:33], v[216:223], v[78:81], v188, v189 op_sel_hi:[0,0,0]
	v_mfma_scale_f32_16x16x128_f8f6f4 v[74:77], v[18:25], v[216:223], v[74:77], v188, v189 op_sel_hi:[0,0,0]
	v_mfma_scale_f32_16x16x128_f8f6f4 v[62:65], v[26:33], v[224:231], v[62:65], v188, v189 op_sel_hi:[0,0,0]
	v_mfma_scale_f32_16x16x128_f8f6f4 v[58:61], v[18:25], v[224:231], v[58:61], v188, v189 op_sel_hi:[0,0,0]
	v_mfma_scale_f32_16x16x128_f8f6f4 v[46:49], v[26:33], v[232:239], v[46:49], v188, v189 op_sel_hi:[0,0,0]
	v_mfma_scale_f32_16x16x128_f8f6f4 v[42:45], v[18:25], v[232:239], v[42:45], v188, v189 op_sel_hi:[0,0,0]
	s_setprio 0
	s_setprio 1
	v_mfma_scale_f32_16x16x128_f8f6f4 v[86:89], v[10:17], v[208:215], v[86:89], v188, v189 op_sel_hi:[0,0,0]
	v_mfma_scale_f32_16x16x128_f8f6f4 v[82:85], v[2:9], v[208:215], v[82:85], v188, v189 op_sel_hi:[0,0,0]
	v_mfma_scale_f32_16x16x128_f8f6f4 v[70:73], v[10:17], v[216:223], v[70:73], v188, v189 op_sel_hi:[0,0,0]
	v_mfma_scale_f32_16x16x128_f8f6f4 v[66:69], v[2:9], v[216:223], v[66:69], v188, v189 op_sel_hi:[0,0,0]
	v_mfma_scale_f32_16x16x128_f8f6f4 v[54:57], v[10:17], v[224:231], v[54:57], v188, v189 op_sel_hi:[0,0,0]
	v_mfma_scale_f32_16x16x128_f8f6f4 v[50:53], v[2:9], v[224:231], v[50:53], v188, v189 op_sel_hi:[0,0,0]
	v_mfma_scale_f32_16x16x128_f8f6f4 v[38:41], v[10:17], v[232:239], v[38:41], v188, v189 op_sel_hi:[0,0,0]
	v_mfma_scale_f32_16x16x128_f8f6f4 v[34:37], v[2:9], v[232:239], v[34:37], v188, v189 op_sel_hi:[0,0,0]
	s_setprio 0
	s_barrier
	s_add_u32 s34, s34, 0x100
	s_addc_u32 s35, s35, 0
	s_add_u32 s36, s36, 0x100
	s_addc_u32 s37, s37, 0
	s_cmp_ge_i32 s23, s49
	s_cbranch_scc1 .LBB0_1444
	s_branch .LBB0_1443

.LBB0_1446:
	v_readfirstlane_b32 s70, v0
	s_lshr_b32 s70, s70, 6
	s_cmp_eq_u64 s[2:3], 0
	s_cselect_b32 s71, s65, s66
	s_lshl_b32 s71, s71, 17
	s_lshl_b32 s72, s28, 14
	s_add_u32 s71, s71, s72
	s_and_b32 s72, s70, 1
	s_lshl_b32 s72, s72, 13
	s_add_u32 s71, s71, s72
	s_add_u32 s74, s12, s71
	s_addc_u32 s75, s13, 0
	s_bfe_u32 s72, s80, 0x20006
	s_lshl_b32 s72, s72, 15
	s_sub_u32 s73, s70, 2
	s_lshl_b32 s78, s73, 13
	s_add_u32 s72, s72, s78
	s_add_u32 s76, s26, s72
	s_addc_u32 s77, s27, 0
	s_cmp_lt_u32 s73, 4
	s_cselect_b64 s[74:75], s[76:77], s[74:75]
	v_lshlrev_b32_e32 v250, 7, v206
	global_load_dword v251, v250, s[74:75]
	v_lshl_or_b32 v10, s28, 8, v190
	v_max_f32_e32 v2, v158, v158
	v_med3_f32 v3, v2, s64, v196
	v_max_f32_e32 v2, v159, v159
	v_med3_f32 v4, v2, s64, v196
	v_mov_b32_e32 v2, v169
	v_cvt_pk_fp8_f32 v2, v3, v4
	v_max_f32_e32 v5, v160, v160
	v_max_f32_e32 v4, v161, v161
	v_med3_f32 v3, v5, s64, v196
	v_med3_f32 v4, v4, s64, v196
	v_cvt_pk_fp8_f32 v2, v3, v4 op_sel:[0,0,1]
	v_max_f32_e32 v3, v154, v154
	v_med3_f32 v4, v3, s64, v196
	v_max_f32_e32 v3, v155, v155
	v_med3_f32 v5, v3, s64, v196
	v_mov_b32_e32 v3, v169
	v_cvt_pk_fp8_f32 v3, v4, v5
	v_max_f32_e32 v6, v156, v156
	v_max_f32_e32 v5, v157, v157
	v_med3_f32 v4, v6, s64, v196
	v_med3_f32 v5, v5, s64, v196
	v_cvt_pk_fp8_f32 v3, v4, v5 op_sel:[0,0,1]
	v_max_f32_e32 v4, v150, v150
	v_med3_f32 v5, v4, s64, v196
	v_max_f32_e32 v4, v151, v151
	v_med3_f32 v6, v4, s64, v196
	v_mov_b32_e32 v4, v169
	v_cvt_pk_fp8_f32 v4, v5, v6
	v_max_f32_e32 v7, v152, v152
	v_max_f32_e32 v6, v153, v153
	v_med3_f32 v5, v7, s64, v196
	v_med3_f32 v6, v6, s64, v196
	v_cvt_pk_fp8_f32 v4, v5, v6 op_sel:[0,0,1]
	v_max_f32_e32 v5, v146, v146
	v_med3_f32 v6, v5, s64, v196
	v_max_f32_e32 v5, v147, v147
	v_med3_f32 v7, v5, s64, v196
	v_mov_b32_e32 v5, v169
	v_cvt_pk_fp8_f32 v5, v6, v7
	v_max_f32_e32 v8, v148, v148
	v_max_f32_e32 v7, v149, v149
	v_med3_f32 v6, v8, s64, v196
	v_med3_f32 v7, v7, s64, v196
	v_cvt_pk_fp8_f32 v5, v6, v7 op_sel:[0,0,1]
	v_max_f32_e32 v6, v142, v142
	v_med3_f32 v7, v6, s64, v196
	v_max_f32_e32 v6, v143, v143
	v_med3_f32 v8, v6, s64, v196
	v_mov_b32_e32 v6, v169
	v_cvt_pk_fp8_f32 v6, v7, v8
	v_max_f32_e32 v9, v144, v144
	v_max_f32_e32 v8, v145, v145
	v_med3_f32 v7, v9, s64, v196
	v_med3_f32 v8, v8, s64, v196
	v_cvt_pk_fp8_f32 v6, v7, v8 op_sel:[0,0,1]
	v_max_f32_e32 v7, v138, v138
	v_med3_f32 v8, v7, s64, v196
	v_max_f32_e32 v7, v139, v139
	v_med3_f32 v9, v7, s64, v196
	v_mov_b32_e32 v7, v169
	v_cvt_pk_fp8_f32 v7, v8, v9
	v_max_f32_e32 v11, v140, v140
	v_max_f32_e32 v9, v141, v141
	v_med3_f32 v8, v11, s64, v196
	v_med3_f32 v9, v9, s64, v196
	v_cvt_pk_fp8_f32 v7, v8, v9 op_sel:[0,0,1]
	v_max_f32_e32 v8, v134, v134
	v_med3_f32 v9, v8, s64, v196
	v_max_f32_e32 v8, v135, v135
	v_med3_f32 v11, v8, s64, v196
	v_mov_b32_e32 v8, v169
	v_cvt_pk_fp8_f32 v8, v9, v11
	v_max_f32_e32 v12, v136, v136
	v_max_f32_e32 v11, v137, v137
	v_med3_f32 v9, v12, s64, v196
	v_med3_f32 v11, v11, s64, v196
	v_cvt_pk_fp8_f32 v8, v9, v11 op_sel:[0,0,1]
	v_max_f32_e32 v9, v130, v130
	v_med3_f32 v11, v9, s64, v196
	v_max_f32_e32 v9, v131, v131
	v_med3_f32 v12, v9, s64, v196
	v_mov_b32_e32 v9, v169
	v_cvt_pk_fp8_f32 v9, v11, v12
	v_max_f32_e32 v13, v132, v132
	v_max_f32_e32 v12, v133, v133
	v_med3_f32 v11, v13, s64, v196
	v_med3_f32 v12, v12, s64, v196
	v_cvt_pk_fp8_f32 v9, v11, v12 op_sel:[0,0,1]
	s_lshl_b32 s23, s66, 19
	v_add3_u32 v10, s23, v171, v10
	buffer_store_dwordx4 v[2:5], v10, s[4:7], 0 offen
	v_max_f32_e32 v11, v108, v108
	v_max_f32_e32 v12, v104, v104
	v_add_u32_e32 v2, 0x8000, v10
	buffer_store_dwordx4 v[6:9], v2, s[4:7], 0 offen
	v_max_f32_e32 v2, v126, v126
	v_med3_f32 v3, v2, s64, v196
	v_max_f32_e32 v2, v127, v127
	v_med3_f32 v4, v2, s64, v196
	v_mov_b32_e32 v2, v169
	v_cvt_pk_fp8_f32 v2, v3, v4
	v_max_f32_e32 v5, v128, v128
	v_max_f32_e32 v4, v129, v129
	v_med3_f32 v3, v5, s64, v196
	v_med3_f32 v4, v4, s64, v196
	v_cvt_pk_fp8_f32 v2, v3, v4 op_sel:[0,0,1]
	v_max_f32_e32 v3, v122, v122
	v_med3_f32 v4, v3, s64, v196
	v_max_f32_e32 v3, v123, v123
	v_med3_f32 v5, v3, s64, v196
	v_mov_b32_e32 v3, v169
	v_cvt_pk_fp8_f32 v3, v4, v5
	v_max_f32_e32 v6, v124, v124
	v_max_f32_e32 v5, v125, v125
	v_med3_f32 v4, v6, s64, v196
	v_med3_f32 v5, v5, s64, v196
	v_cvt_pk_fp8_f32 v3, v4, v5 op_sel:[0,0,1]
	v_max_f32_e32 v4, v118, v118
	v_med3_f32 v5, v4, s64, v196
	v_max_f32_e32 v4, v119, v119
	v_med3_f32 v6, v4, s64, v196
	v_mov_b32_e32 v4, v169
	v_cvt_pk_fp8_f32 v4, v5, v6
	v_max_f32_e32 v7, v120, v120
	v_max_f32_e32 v6, v121, v121
	v_med3_f32 v5, v7, s64, v196
	v_med3_f32 v6, v6, s64, v196
	v_cvt_pk_fp8_f32 v4, v5, v6 op_sel:[0,0,1]
	v_max_f32_e32 v5, v114, v114
	v_med3_f32 v6, v5, s64, v196
	v_max_f32_e32 v5, v115, v115
	v_med3_f32 v7, v5, s64, v196
	v_mov_b32_e32 v5, v169
	v_cvt_pk_fp8_f32 v5, v6, v7
	v_max_f32_e32 v8, v116, v116
	v_max_f32_e32 v7, v117, v117
	v_med3_f32 v6, v8, s64, v196
	v_med3_f32 v7, v7, s64, v196
	v_cvt_pk_fp8_f32 v5, v6, v7 op_sel:[0,0,1]
	v_max_f32_e32 v6, v110, v110
	v_med3_f32 v7, v6, s64, v196
	v_max_f32_e32 v6, v111, v111
	v_med3_f32 v8, v6, s64, v196
	v_mov_b32_e32 v6, v169
	v_cvt_pk_fp8_f32 v6, v7, v8
	v_max_f32_e32 v9, v112, v112
	v_max_f32_e32 v8, v113, v113
	v_med3_f32 v7, v9, s64, v196
	v_med3_f32 v8, v8, s64, v196
	v_cvt_pk_fp8_f32 v6, v7, v8 op_sel:[0,0,1]
	v_max_f32_e32 v7, v106, v106
	v_med3_f32 v8, v7, s64, v196
	v_max_f32_e32 v7, v107, v107
	v_med3_f32 v9, v7, s64, v196
	v_mov_b32_e32 v7, v169
	v_cvt_pk_fp8_f32 v7, v8, v9
	v_max_f32_e32 v9, v109, v109
	v_med3_f32 v8, v11, s64, v196
	v_med3_f32 v9, v9, s64, v196
	v_cvt_pk_fp8_f32 v7, v8, v9 op_sel:[0,0,1]
	v_max_f32_e32 v8, v102, v102
	v_med3_f32 v9, v8, s64, v196
	v_max_f32_e32 v8, v103, v103
	v_med3_f32 v11, v8, s64, v196
	v_mov_b32_e32 v8, v169
	v_cvt_pk_fp8_f32 v8, v9, v11
	v_max_f32_e32 v11, v105, v105
	v_med3_f32 v9, v12, s64, v196
	v_med3_f32 v11, v11, s64, v196
	v_cvt_pk_fp8_f32 v8, v9, v11 op_sel:[0,0,1]
	v_max_f32_e32 v9, v98, v98
	v_med3_f32 v11, v9, s64, v196
	v_max_f32_e32 v9, v99, v99
	v_med3_f32 v12, v9, s64, v196
	v_mov_b32_e32 v9, v169
	v_cvt_pk_fp8_f32 v9, v11, v12
	v_max_f32_e32 v13, v100, v100
	v_max_f32_e32 v12, v101, v101
	v_med3_f32 v11, v13, s64, v196
	v_med3_f32 v12, v12, s64, v196
	v_cvt_pk_fp8_f32 v9, v11, v12 op_sel:[0,0,1]
	v_add_u32_e32 v11, 0x10000, v10
	buffer_store_dwordx4 v[2:5], v11, s[4:7], 0 offen
	v_max_f32_e32 v11, v76, v76
	v_max_f32_e32 v12, v72, v72
	v_add_u32_e32 v2, 0x18000, v10
	buffer_store_dwordx4 v[6:9], v2, s[4:7], 0 offen
	v_max_f32_e32 v2, v94, v94
	v_med3_f32 v3, v2, s64, v196
	v_max_f32_e32 v2, v95, v95
	v_med3_f32 v4, v2, s64, v196
	v_mov_b32_e32 v2, v169
	v_cvt_pk_fp8_f32 v2, v3, v4
	v_max_f32_e32 v5, v96, v96
	v_max_f32_e32 v4, v97, v97
	v_med3_f32 v3, v5, s64, v196
	v_med3_f32 v4, v4, s64, v196
	v_cvt_pk_fp8_f32 v2, v3, v4 op_sel:[0,0,1]
	v_max_f32_e32 v3, v90, v90
	v_med3_f32 v4, v3, s64, v196
	v_max_f32_e32 v3, v91, v91
	v_med3_f32 v5, v3, s64, v196
	v_mov_b32_e32 v3, v169
	v_cvt_pk_fp8_f32 v3, v4, v5
	v_max_f32_e32 v6, v92, v92
	v_max_f32_e32 v5, v93, v93
	v_med3_f32 v4, v6, s64, v196
	v_med3_f32 v5, v5, s64, v196
	v_cvt_pk_fp8_f32 v3, v4, v5 op_sel:[0,0,1]
	v_max_f32_e32 v4, v86, v86
	v_med3_f32 v5, v4, s64, v196
	v_max_f32_e32 v4, v87, v87
	v_med3_f32 v6, v4, s64, v196
	v_mov_b32_e32 v4, v169
	v_cvt_pk_fp8_f32 v4, v5, v6
	v_max_f32_e32 v7, v88, v88
	v_max_f32_e32 v6, v89, v89
	v_med3_f32 v5, v7, s64, v196
	v_med3_f32 v6, v6, s64, v196
	v_cvt_pk_fp8_f32 v4, v5, v6 op_sel:[0,0,1]
	v_max_f32_e32 v5, v82, v82
	v_med3_f32 v6, v5, s64, v196
	v_max_f32_e32 v5, v83, v83
	v_med3_f32 v7, v5, s64, v196
	v_mov_b32_e32 v5, v169
	v_cvt_pk_fp8_f32 v5, v6, v7
	v_max_f32_e32 v8, v84, v84
	v_max_f32_e32 v7, v85, v85
	v_med3_f32 v6, v8, s64, v196
	v_med3_f32 v7, v7, s64, v196
	v_cvt_pk_fp8_f32 v5, v6, v7 op_sel:[0,0,1]
	v_max_f32_e32 v6, v78, v78
	v_med3_f32 v7, v6, s64, v196
	v_max_f32_e32 v6, v79, v79
	v_med3_f32 v8, v6, s64, v196
	v_mov_b32_e32 v6, v169
	v_cvt_pk_fp8_f32 v6, v7, v8
	v_max_f32_e32 v9, v80, v80
	v_max_f32_e32 v8, v81, v81
	v_med3_f32 v7, v9, s64, v196
	v_med3_f32 v8, v8, s64, v196
	v_cvt_pk_fp8_f32 v6, v7, v8 op_sel:[0,0,1]
	v_max_f32_e32 v7, v74, v74
	v_med3_f32 v8, v7, s64, v196
	v_max_f32_e32 v7, v75, v75
	v_med3_f32 v9, v7, s64, v196
	v_mov_b32_e32 v7, v169
	v_cvt_pk_fp8_f32 v7, v8, v9
	v_max_f32_e32 v9, v77, v77
	v_med3_f32 v8, v11, s64, v196
	v_med3_f32 v9, v9, s64, v196
	v_cvt_pk_fp8_f32 v7, v8, v9 op_sel:[0,0,1]
	v_max_f32_e32 v8, v70, v70
	v_med3_f32 v9, v8, s64, v196
	v_max_f32_e32 v8, v71, v71
	v_med3_f32 v11, v8, s64, v196
	v_mov_b32_e32 v8, v169
	v_cvt_pk_fp8_f32 v8, v9, v11
	v_max_f32_e32 v11, v73, v73
	v_med3_f32 v9, v12, s64, v196
	v_med3_f32 v11, v11, s64, v196
	v_cvt_pk_fp8_f32 v8, v9, v11 op_sel:[0,0,1]
	v_max_f32_e32 v9, v66, v66
	v_med3_f32 v11, v9, s64, v196
	v_max_f32_e32 v9, v67, v67
	v_med3_f32 v12, v9, s64, v196
	v_mov_b32_e32 v9, v169
	v_cvt_pk_fp8_f32 v9, v11, v12
	v_max_f32_e32 v13, v68, v68
	v_max_f32_e32 v12, v69, v69
	v_med3_f32 v11, v13, s64, v196
	v_med3_f32 v12, v12, s64, v196
	v_cvt_pk_fp8_f32 v9, v11, v12 op_sel:[0,0,1]
	v_add_u32_e32 v11, 0x40000, v10
	buffer_store_dwordx4 v[2:5], v11, s[4:7], 0 offen
	v_max_f32_e32 v11, v44, v44
	v_max_f32_e32 v12, v40, v40
	v_add_u32_e32 v2, 0x48000, v10
	buffer_store_dwordx4 v[6:9], v2, s[4:7], 0 offen
	v_max_f32_e32 v2, v62, v62
	v_med3_f32 v3, v2, s64, v196
	v_max_f32_e32 v2, v63, v63
	v_med3_f32 v4, v2, s64, v196
	v_mov_b32_e32 v2, v169
	v_cvt_pk_fp8_f32 v2, v3, v4
	v_max_f32_e32 v5, v64, v64
	v_max_f32_e32 v4, v65, v65
	v_med3_f32 v3, v5, s64, v196
	v_med3_f32 v4, v4, s64, v196
	v_cvt_pk_fp8_f32 v2, v3, v4 op_sel:[0,0,1]
	v_max_f32_e32 v3, v58, v58
	v_med3_f32 v4, v3, s64, v196
	v_max_f32_e32 v3, v59, v59
	v_med3_f32 v5, v3, s64, v196
	v_mov_b32_e32 v3, v169
	v_cvt_pk_fp8_f32 v3, v4, v5
	v_max_f32_e32 v6, v60, v60
	v_max_f32_e32 v5, v61, v61
	v_med3_f32 v4, v6, s64, v196
	v_med3_f32 v5, v5, s64, v196
	v_cvt_pk_fp8_f32 v3, v4, v5 op_sel:[0,0,1]
	v_max_f32_e32 v4, v54, v54
	v_med3_f32 v5, v4, s64, v196
	v_max_f32_e32 v4, v55, v55
	v_med3_f32 v6, v4, s64, v196
	v_mov_b32_e32 v4, v169
	v_cvt_pk_fp8_f32 v4, v5, v6
	v_max_f32_e32 v7, v56, v56
	v_max_f32_e32 v6, v57, v57
	v_med3_f32 v5, v7, s64, v196
	v_med3_f32 v6, v6, s64, v196
	v_cvt_pk_fp8_f32 v4, v5, v6 op_sel:[0,0,1]
	v_max_f32_e32 v5, v50, v50
	v_med3_f32 v6, v5, s64, v196
	v_max_f32_e32 v5, v51, v51
	v_med3_f32 v7, v5, s64, v196
	v_mov_b32_e32 v5, v169
	v_cvt_pk_fp8_f32 v5, v6, v7
	v_max_f32_e32 v8, v52, v52
	v_max_f32_e32 v7, v53, v53
	v_med3_f32 v6, v8, s64, v196
	v_med3_f32 v7, v7, s64, v196
	v_cvt_pk_fp8_f32 v5, v6, v7 op_sel:[0,0,1]
	v_max_f32_e32 v6, v46, v46
	v_med3_f32 v7, v6, s64, v196
	v_max_f32_e32 v6, v47, v47
	v_med3_f32 v8, v6, s64, v196
	v_mov_b32_e32 v6, v169
	v_cvt_pk_fp8_f32 v6, v7, v8
	v_max_f32_e32 v9, v48, v48
	v_max_f32_e32 v8, v49, v49
	v_med3_f32 v7, v9, s64, v196
	v_med3_f32 v8, v8, s64, v196
	v_cvt_pk_fp8_f32 v6, v7, v8 op_sel:[0,0,1]
	v_max_f32_e32 v7, v42, v42
	v_med3_f32 v8, v7, s64, v196
	v_max_f32_e32 v7, v43, v43
	v_med3_f32 v9, v7, s64, v196
	v_mov_b32_e32 v7, v169
	v_cvt_pk_fp8_f32 v7, v8, v9
	v_max_f32_e32 v9, v45, v45
	v_med3_f32 v8, v11, s64, v196
	v_med3_f32 v9, v9, s64, v196
	v_cvt_pk_fp8_f32 v7, v8, v9 op_sel:[0,0,1]
	v_max_f32_e32 v8, v38, v38
	v_med3_f32 v9, v8, s64, v196
	v_max_f32_e32 v8, v39, v39
	v_med3_f32 v11, v8, s64, v196
	v_mov_b32_e32 v8, v169
	v_cvt_pk_fp8_f32 v8, v9, v11
	v_max_f32_e32 v11, v41, v41
	v_med3_f32 v9, v12, s64, v196
	v_med3_f32 v11, v11, s64, v196
	v_cvt_pk_fp8_f32 v8, v9, v11 op_sel:[0,0,1]
	v_max_f32_e32 v9, v34, v34
	v_med3_f32 v11, v9, s64, v196
	v_max_f32_e32 v9, v35, v35
	v_med3_f32 v12, v9, s64, v196
	v_mov_b32_e32 v9, v169
	v_cvt_pk_fp8_f32 v9, v11, v12
	v_max_f32_e32 v13, v36, v36
	v_max_f32_e32 v12, v37, v37
	v_med3_f32 v11, v13, s64, v196
	v_med3_f32 v12, v12, s64, v196
	v_cvt_pk_fp8_f32 v9, v11, v12 op_sel:[0,0,1]
	v_add_u32_e32 v11, 0x50000, v10
	buffer_store_dwordx4 v[2:5], v11, s[4:7], 0 offen
	s_and_b64 vcc, exec, s[2:3]
	s_mov_b64 s[2:3], -1
	v_add_u32_e32 v2, 0x58000, v10
	buffer_store_dwordx4 v[6:9], v2, s[4:7], 0 offen
	s_mov_b32 s98, 1
	s_cbranch_vccnz .LBB0_1436
	s_andn2_b64 vcc, exec, s[14:15]
	s_cbranch_vccnz .LBB0_1435
	s_barrier
	s_branch .LBB0_1435
